# attn_dsa QK: second batch's LDS reads issued behind the first batch's MFMAs, counted lgkmcnt waits, on top of v89
# speedup vs baseline: 1.0096x; 1.0027x over previous
.LBB0_1225:
	s_bitcmp1_b32 s24, 0
	s_cselect_b32 s0, 0x8900, 0
	s_add_i32 s24, s72, s0
	v_add3_u32 v203, s24, v168, v148
	ds_read_b128 v[68:71], v203
	ds_read_b128 v[182:185], v203 offset:32
	ds_read_b128 v[72:75], v203 offset:8704
	ds_read_b128 v[186:189], v203 offset:8736
	ds_read_b128 v[190:193], v203 offset:64
	ds_read_b128 v[204:207], v203 offset:96
	ds_read_b128 v[208:211], v203 offset:8768
	ds_read_b128 v[212:215], v203 offset:8800
	ds_read_b128 v[216:219], v203 offset:8896
	ds_read_b128 v[220:223], v203 offset:8928
	s_waitcnt lgkmcnt(9)
	v_mfma_f32_32x32x16_bf16 v[84:99], v[68:71], v[100:103], 0
	s_waitcnt lgkmcnt(7)
	v_mfma_f32_32x32x16_bf16 v[68:83], v[72:75], v[100:103], 0
	v_mfma_f32_32x32x16_bf16 v[84:99], v[182:185], v[104:107], v[84:99]
	ds_read_b128 v[182:185], v203 offset:128
	s_waitcnt lgkmcnt(7)
	v_mfma_f32_32x32x16_bf16 v[68:83], v[186:189], v[104:107], v[68:83]
	ds_read_b128 v[186:189], v203 offset:160
	s_waitcnt lgkmcnt(7)
	v_mfma_f32_32x32x16_bf16 v[84:99], v[190:193], v[108:111], v[84:99]
	ds_read_b128 v[190:193], v203 offset:8832
	s_waitcnt lgkmcnt(6)
	v_mfma_f32_32x32x16_bf16 v[68:83], v[208:211], v[108:111], v[68:83]
	ds_read_b128 v[208:211], v203 offset:192
	v_mfma_f32_32x32x16_bf16 v[84:99], v[204:207], v[112:115], v[84:99]
	ds_read_b128 v[204:207], v203 offset:8864
	s_waitcnt lgkmcnt(7)
	v_mfma_f32_32x32x16_bf16 v[68:83], v[212:215], v[112:115], v[68:83]
	ds_read_b128 v[212:215], v203 offset:224
	s_waitcnt lgkmcnt(5)
	v_mfma_f32_32x32x16_bf16 v[84:99], v[182:185], v[116:119], v[84:99]
	s_waitcnt lgkmcnt(3)
	v_mfma_f32_32x32x16_bf16 v[68:83], v[190:193], v[116:119], v[68:83]
	v_mfma_f32_32x32x16_bf16 v[84:99], v[186:189], v[120:123], v[84:99]
	s_waitcnt lgkmcnt(1)
	v_mfma_f32_32x32x16_bf16 v[68:83], v[204:207], v[120:123], v[68:83]
	v_mfma_f32_32x32x16_bf16 v[84:99], v[208:211], v[124:127], v[84:99]
	v_mfma_f32_32x32x16_bf16 v[68:83], v[216:219], v[124:127], v[68:83]
	s_waitcnt lgkmcnt(0)
	v_mfma_f32_32x32x16_bf16 v[84:99], v[212:215], v[128:131], v[84:99]
	v_mfma_f32_32x32x16_bf16 v[68:83], v[220:223], v[128:131], v[68:83]
	v_mov_b32_e32 v182, s21
	ds_read_b32 v203, v182 offset:2048
	s_cmpk_lt_i32 s20, 0x71
	s_cselect_b64 s[14:15], -1, 0
	s_cmpk_gt_i32 s20, 0x70
	s_waitcnt lgkmcnt(0)
	v_mov_b32_e32 v205, v203
	v_mov_b32_e32 v204, v203
	s_cbranch_scc1 .Ldsa_far
	v_add3_u32 v205, v201, s20, 63
	s_movk_i32 s0, 0x80
	v_cmp_gt_i32_e32 vcc, s0, v205
	v_mov_b32_e32 v204, v203
	s_and_saveexec_b64 s[0:1], vcc
	v_max_i32_e32 v182, 0, v205
	v_lshl_add_u32 v182, v182, 2, s22
	ds_read_b32 v204, v182
	s_or_b64 exec, exec, s[0:1]
	v_min_i32_e32 v182, 0xa0, v205
	v_subrev_u32_e32 v182, 32, v182
	v_cmp_lt_i32_e32 vcc, 31, v205
	s_movk_i32 s0, 0x80
	v_mov_b32_e32 v205, v203
	v_cndmask_b32_e32 v206, 0, v182, vcc
	v_cmp_ne_u32_e32 vcc, s0, v206
	s_and_saveexec_b64 s[0:1], vcc
	v_lshl_add_u32 v182, v206, 2, s22
	ds_read_b32 v205, v182
	s_or_b64 exec, exec, s[0:1]
